# T10c + release-flag check before each seam-0 unit (the front-loading stops if the barrier has already released; leftovers drain at seam 14)
# speedup vs baseline: 1.0114x; 1.0008x over previous
; __device__ __forceinline__ void transpose_item_f8(const float* W, int N, unsigned char* WT, int ldt, int kind, int off, int item, int lane, float scale) {
;     const int nblk = N >> 6, kb = item / nblk, nb = item - kb * nblk, k0 = 128 * kb + 16 * (lane & 7), n = 64 * nb + 4 * (lane >> 3);
; __device__ __forceinline__ void moe_convert(Frame& F, int lo, int hi, int rank, int nrank) {
;     ...
;     for (int it = lo + rank; it < hi; it += nrank) {
;         int r = it; const float* W; unsigned char* WT; int N, ldt, kind, off; float f8s;
;         if (r < 14336) { const int e = r / 1792; r -= e * 1792; W = F.in[IN_WMG] + (size_t)e * 2048 * DFFE; N = DFFE; WT = F.ws + WS_WGU1 + (size_t)e * 14336 * 2048; ldt = 2048; kind = 1; off = 0; f8s = 32.f; }
;         else if ((r -= 14336) < 14336) { const int e = r / 1792; r -= e * 1792; W = F.in[IN_WMU] + (size_t)e * 2048 * DFFE; N = DFFE; WT = F.ws + WS_WGU1 + (size_t)e * 14336 * 2048; ldt = 2048; kind = 1; off = 128; f8s = 256.f; }
;         else { r -= 14336; const int e = r / 1792; r -= e * 1792; W = F.in[IN_WMD] + (size_t)e * DFFE * 2048; N = 2048; WT = F.ws + WS_WDN1 + (size_t)e * 2048 * DFFE; ldt = DFFE; kind = 0; off = 0; f8s = 64.f; }
;         transpose_item_f8(W, N, WT, ldt, kind, off, r, F.lane, f8s);
.Lsf0_loop:
	ds_read_b32 v9, v8
	s_waitcnt lgkmcnt(0)
	v_readfirstlane_b32 s5, v9
	s_cmp_eq_u32 s5, 1
	s_cbranch_scc1 .Lsf0_done
	ds_add_rtn_u32 v9, v8, v18 offset:4
	s_waitcnt lgkmcnt(0)
	v_readfirstlane_b32 s18, v9
	s_cmp_ge_u32 s18, s40
	s_cbranch_scc1 .Lsf0_done
	s_add_i32 s18, s18, s33
	s_and_b32 s27, s18, 1
	s_lshr_b32 s19, s18, 1
	s_add_i32 s19, s19, 0x5000
	s_cmp_lt_u32 s19, 0x7000
	s_cbranch_scc0 .Lsf0_down
	s_add_i32 s20, s19, 0xffffc800
	s_lshr_b32 s21, s20, 8
	s_mul_i32 s21, s21, 37
	s_lshr_b32 s21, s21, 8
	s_mul_i32 s28, s21, 0x700
	s_sub_i32 s20, s20, s28
	s_mul_i32 s28, s21, 0x3800000
	s_add_u32 s14, s10, s28
	s_addc_u32 s15, s11, 0
	s_mul_i32 s28, s21, 0x1c00000
	s_add_u32 s28, s28, 0x7800000
	s_add_u32 s16, s86, s28
	s_addc_u32 s17, s87, 0
	s_movk_i32 s24, 0x7000
	s_movk_i32 s25, 0x800
	s_mov_b32 s26, 0x43800000
	s_lshr_b32 s22, s20, 4
	s_mul_i32 s22, s22, 0x2493
	s_lshr_b32 s22, s22, 16
	s_mul_i32 s28, s22, 0x70
	s_sub_i32 s23, s20, s28
	s_mov_b32 s29, 1
	s_branch .Lsf0_dec
